# speedup vs baseline: 1.1036x; 1.0552x over previous
.LBB5_15:
	s_or_b64 exec, exec, s[6:7]
	s_load_dwordx4 s[4:7], s[0:1], 0x18
	v_mov_b32_e32 v17, 0
	s_waitcnt lgkmcnt(0)
	s_barrier
	ds_read_b32 v17, v17 offset:32776
	s_and_b32 s17, s5, 0xffff
	s_and_b32 s21, s15, 0xffff
	v_accvgpr_read_b32 v56, a0
	v_lshlrev_b32_e32 v15, 12, v1
	v_lshlrev_b32_e32 v18, 4, v56
	s_add_u32 s8, s4, s7
	s_mov_b32 s16, s4
	v_lshlrev_b32_e32 v14, 14, v10
	v_lshlrev_b32_e32 v16, 7, v0
	s_addc_u32 s9, s5, 0
	s_waitcnt lgkmcnt(0)
	v_cmp_ne_u32_e64 s[4:5], 0, v17
	v_add_u32_e32 v17, 0, v15
	v_or_b32_e32 v15, v18, v15
	v_or3_b32 v15, v16, v14, v15
	v_lshlrev_b32_e32 v13, 3, v0
	v_accvgpr_write_b32 a98, v15
	v_and_b32_e32 v15, 63, v57
	v_lshlrev_b32_e32 v19, 4, v13
	v_lshrrev_b32_e32 v15, 5, v15
	s_waitcnt vmcnt(1)
	v_mul_f32_e32 v45, 0xbfb8aa3b, v6
	v_mul_f32_e32 v6, 0xbfb8aa3b, v7
	v_mul_f32_e32 v7, 0xbfb8aa3b, v9
	v_lshlrev_b32_e32 v9, 8, v1
	v_add3_u32 v17, v17, v19, v18
	v_accvgpr_write_b32 a94, v15
	v_bfe_u32 v16, v57, 2, 3
	v_lshlrev_b32_e32 v15, 3, v57
	v_add_u32_e32 v9, v23, v9
	v_accvgpr_write_b32 a97, v17
	v_and_b32_e32 v17, 24, v15
	v_lshlrev_b32_e32 v10, 13, v10
	v_lshlrev_b32_e32 v15, 10, v16
	v_or_b32_e32 v9, v9, v13
	v_or3_b32 v10, v10, v15, v17
	v_cmp_eq_u32_e64 s[2:3], 3, v1
	v_lshl_add_u32 v9, v9, 1, s6
	v_accvgpr_write_b32 a95, v16
	v_lshl_add_u32 v16, v10, 1, s44
	v_lshlrev_b32_e32 v1, 7, v1
	v_and_b32_e32 v10, 8, v57
	v_lshlrev_b32_e32 v0, 1, v0
	v_or3_b32 v1, v1, v10, v0
	v_add_u32_e32 v10, s24, v9
	s_lshl_b32 s6, s33, 9
	v_or3_b32 v1, v1, v18, v14
	v_accvgpr_write_b32 a99, v10
	v_add_u32_e32 v10, s26, v9
	v_add_u32_e32 v1, s6, v1
	s_and_b32 s33, s6, 0xe00
	s_lshl_b32 s6, s42, 9
	v_accvgpr_write_b32 a102, v10
	v_add_u32_e32 v10, s28, v9
	s_and_b32 s35, s6, 0xe00
	s_lshl_b32 s6, s43, 9
	v_accvgpr_write_b32 a103, v10
	v_add_u32_e32 v10, s30, v9
	s_and_b32 s37, s6, 0xe00
	s_lshl_b32 s6, s45, 9
	v_accvgpr_write_b32 a104, v10
	v_add_u32_e32 v10, s34, v9
	v_accvgpr_write_b32 a96, v17
	v_ashrrev_i32_e32 v17, 31, v16
	s_and_b32 s39, s6, 0xe00
	s_lshl_b32 s6, s46, 9
	v_accvgpr_write_b32 a105, v10
	v_add_u32_e32 v10, s36, v9
	v_accvgpr_write_b32 a93, v17
	s_and_b32 s41, s6, 0xe00
	s_lshl_b32 s6, s47, 9
	v_accvgpr_write_b32 a106, v10
	v_add_u32_e32 v10, s38, v9
	v_add_u32_e32 v9, s40, v9
	v_or_b32_e32 v13, v13, v56
	v_accvgpr_write_b32 a92, v16
	v_lshl_add_u64 v[16:17], s[8:9], 0, v[16:17]
	s_and_b32 s42, s6, 0xe00
	s_lshl_b32 s6, s48, 9
	v_accvgpr_write_b32 a108, v9
	v_lshlrev_b32_e32 v9, 1, v12
	s_mov_b32 s19, 0x20000
	v_accvgpr_write_b32 a101, v17
	s_and_b32 s43, s6, 0xe00
	s_lshl_b32 s6, s49, 9
	v_accvgpr_write_b32 a107, v10
	v_add3_u32 v0, 0, v9, v0
	v_lshlrev_b32_e32 v9, 9, v11
	v_lshlrev_b32_e32 v10, 4, v13
	s_brev_b32 s18, -2
	s_mov_b32 s22, 0x80000
	s_mov_b32 s23, s19
	s_mov_b32 s20, s14
	v_cmp_gt_u32_e64 s[0:1], 8, v22
	s_mov_b32 s15, 0
	v_accvgpr_write_b32 a100, v16
	s_and_b32 s44, s6, 0xe00
	v_add3_u32 v9, 0, v9, v10
	s_mov_b64 s[26:27], 0
	s_mov_b32 s34, 0x80008000
	s_mov_b32 s36, 0x100000
	s_brev_b32 s38, 60
	s_mov_b32 s40, 0xbc38aa3b
	s_mov_b32 s45, 0x41000000
	s_waitcnt vmcnt(0)
	v_accvgpr_write_b32 a112, v250
	v_accvgpr_write_b32 a113, v251
	v_accvgpr_write_b32 a114, v252
	v_accvgpr_write_b32 a115, v253
	v_accvgpr_write_b32 a116, v2
	v_accvgpr_write_b32 a117, v3
	v_accvgpr_write_b32 a118, v4
	v_accvgpr_write_b32 a119, v5
	v_and_b32_e32 v46, 8, v57
	v_cmp_ne_u32_e64 s[0:1], 0, v46
	v_and_b32_e32 v46, 32, v57
	v_cmp_ne_u32_e64 s[30:31], 0, v46
	v_mov_b32_e32 v26, 0x44444444
	v_mov_b32_e32 v46, 0xeeeeeeee
	v_cndmask_b32_e64 v26, v26, v46, s[0:1]
	v_accvgpr_read_b32 v46, a98
	v_bfe_u32 v47, v57, 4, 2
	v_lshlrev_b32_e32 v47, 7, v47
	v_sub_u32_e32 v46, v46, v47
	v_bfe_u32 v47, v57, 4, 1
	v_bfe_u32 v48, v57, 3, 1
	v_lshl_or_b32 v47, v47, 1, v48
	v_lshl_add_u32 v46, v47, 7, v46
	v_mov_b32_e32 v47, s33
	v_mov_b32_e32 v48, s35
	v_cndmask_b32_e64 v47, v47, v48, s[30:31]
	v_or_b32_e32 v27, v46, v47
	v_mov_b32_e32 v47, s37
	v_mov_b32_e32 v48, s39
	v_cndmask_b32_e64 v47, v47, v48, s[30:31]
	v_or_b32_e32 v28, v46, v47
	v_mov_b32_e32 v47, s41
	v_mov_b32_e32 v48, s42
	v_cndmask_b32_e64 v47, v47, v48, s[30:31]
	v_or_b32_e32 v29, v46, v47
	v_mov_b32_e32 v47, s43
	v_mov_b32_e32 v48, s44
	v_cndmask_b32_e64 v47, v47, v48, s[30:31]
	v_or_b32_e32 v30, v46, v47
	v_lshrrev_b32_e32 v46, 6, v57
	v_lshlrev_b32_e32 v46, 7, v46
	v_and_b32_e32 v47, 8, v57
	v_bfe_u32 v48, v57, 4, 2
	v_lshl_or_b32 v47, v48, 1, v47
	v_add_u32_e32 v46, v46, v47
	v_sub_u32_e32 v1, v1, v46
	v_bfe_u32 v46, v57, 7, 1
	v_bfe_u32 v47, v57, 5, 1
	v_lshl_or_b32 v46, v46, 1, v47
	v_lshlrev_b32_e32 v46, 7, v46
	v_bfe_u32 v47, v57, 3, 1
	v_bfe_u32 v48, v57, 6, 1
	v_lshl_or_b32 v47, v48, 1, v47
	v_lshl_or_b32 v46, v47, 2, v46
	v_bfe_u32 v47, v57, 4, 1
	v_lshl_or_b32 v46, v47, 1, v46
	v_add_u32_e32 v1, v1, v46
	v_lshrrev_b32_e32 v46, 6, v57
	v_lshlrev_b32_e32 v46, 12, v46
	v_and_b32_e32 v47, 16, v57
	v_lshl_or_b32 v46, v47, 7, v46
	v_lshl_or_b32 v46, v47, 3, v46
	v_and_b32_e32 v47, 32, v57
	v_lshl_or_b32 v46, v47, 3, v46
	v_and_b32_e32 v47, 3, v57
	v_lshl_or_b32 v46, v47, 2, v46
	v_bfe_u32 v47, v57, 2, 2
	v_xor_b32_e32 v48, 0, v47
	v_lshl_or_b32 v48, v48, 4, v46
	v_add_u32_e32 v31, 0, v48
	v_xor_b32_e32 v35, 0x80, v31
	v_xor_b32_e32 v48, 1, v47
	v_lshl_or_b32 v48, v48, 4, v46
	v_add_u32_e32 v32, 512, v48
	v_xor_b32_e32 v36, 0x80, v32
	v_xor_b32_e32 v48, 2, v47
	v_lshl_or_b32 v48, v48, 4, v46
	v_add_u32_e32 v33, 1024, v48
	v_xor_b32_e32 v37, 0x80, v33
	v_xor_b32_e32 v48, 3, v47
	v_lshl_or_b32 v48, v48, 4, v46
	v_add_u32_e32 v34, 1536, v48
	v_xor_b32_e32 v38, 0x80, v34
	v_lshrrev_b32_e32 v46, 3, v57
	v_and_b32_e32 v46, 24, v46
	v_lshrrev_b32_e32 v47, 1, v57
	v_and_or_b32 v46, v47, 4, v46
	v_bfe_u32 v47, v57, 4, 2
	v_or_b32_e32 v46, v46, v47
	v_and_b32_e32 v47, 3, v57
	v_and_b32_e32 v48, 4, v57
	v_lshl_or_b32 v47, v48, 1, v47
	v_xor_b32_e32 v46, v46, v47
	v_and_b32_e32 v47, 7, v57
	v_lshlrev_b32_e32 v47, 9, v47
	v_lshl_or_b32 v9, v46, 4, v47
	v_accvgpr_write_b32 a120, v226
	v_accvgpr_write_b32 a121, v227
	v_accvgpr_write_b32 a122, v228
	v_accvgpr_write_b32 a123, v229
	v_accvgpr_write_b32 a124, v230
	v_accvgpr_write_b32 a125, v231
	v_accvgpr_write_b32 a126, v232
	v_accvgpr_write_b32 a127, v233
	v_accvgpr_write_b32 a128, v234
	v_accvgpr_write_b32 a129, v235
	v_accvgpr_write_b32 a130, v236
	v_accvgpr_write_b32 a131, v237
	v_accvgpr_write_b32 a132, v238
	v_accvgpr_write_b32 a133, v239
	v_accvgpr_write_b32 a134, v240
	v_accvgpr_write_b32 a135, v241
	v_accvgpr_write_b32 a136, v242
	v_accvgpr_write_b32 a137, v243
	v_accvgpr_write_b32 a138, v244
	v_accvgpr_write_b32 a139, v245
	v_accvgpr_write_b32 a140, v246
	v_accvgpr_write_b32 a141, v247
	v_accvgpr_write_b32 a142, v248
	v_accvgpr_write_b32 a143, v249
	s_mov_b64 s[24:25], 0
	s_mov_b32 s46, 0
	s_mov_b32 s30, 0x3c38aa3b
	s_mov_b32 s31, 0xbc000000
	v_bfe_u32 v50, v57, 4, 2
	v_lshlrev_b32_e32 v50, 4, v50
	v_bfe_u32 v51, v57, 4, 1
	v_bfe_u32 v52, v57, 3, 1
	v_lshlrev_b32_e32 v52, 2, v52
	v_lshl_or_b32 v51, v51, 5, v52
	v_sub_u32_e32 v54, v51, v50
	v_and_b32_e32 v55, 32, v57
	v_cmp_ne_u32_e64 s[28:29], 0, v55
	v_accvgpr_read_b32 v242, a99
	v_accvgpr_read_b32 v55, a102
	v_cndmask_b32_e64 v242, v242, v55, s[28:29]
	v_add_u32_e32 v242, v242, v54
	v_accvgpr_read_b32 v243, a103
	v_accvgpr_read_b32 v55, a104
	v_cndmask_b32_e64 v243, v243, v55, s[28:29]
	v_add_u32_e32 v243, v243, v54
	v_accvgpr_read_b32 v244, a105
	v_accvgpr_read_b32 v55, a106
	v_cndmask_b32_e64 v244, v244, v55, s[28:29]
	v_add_u32_e32 v244, v244, v54
	v_accvgpr_read_b32 v245, a107
	v_accvgpr_read_b32 v55, a108
	v_cndmask_b32_e64 v245, v245, v55, s[28:29]
	v_add_u32_e32 v245, v245, v54
	s_mov_b64 s[26:27], -1
	v_mov_b32_e32 v10, 0
	v_mov_b32_e32 v11, 0
	v_mov_b32_e32 v12, 0
	v_mov_b32_e32 v13, 0
	v_mov_b32_e32 v14, 0
	v_mov_b32_e32 v15, 0
	v_mov_b32_e32 v16, 0
	v_mov_b32_e32 v17, 0
	v_mov_b32_e32 v18, 0
	v_mov_b32_e32 v19, 0
	v_mov_b32_e32 v20, 0
	v_mov_b32_e32 v21, 0
	v_mov_b32_e32 v22, 0
	v_mov_b32_e32 v23, 0
	v_mov_b32_e32 v24, 0
	v_mov_b32_e32 v25, 0
	v_mov_b32_e32 v46, 0
	v_mov_b32_e32 v47, 0
	v_mov_b32_e32 v48, 0
	v_mov_b32_e32 v49, 0
	v_mov_b32_e32 v50, 0
	v_mov_b32_e32 v51, 0
	v_mov_b32_e32 v52, 0
	v_mov_b32_e32 v53, 0
	v_mov_b32_e32 v2, 0
	v_mov_b32_e32 v3, 0
	v_mov_b32_e32 v4, 0
	v_mov_b32_e32 v5, 0
	v_mov_b32_e32 v250, 0
	v_mov_b32_e32 v251, 0
	v_mov_b32_e32 v252, 0
	v_mov_b32_e32 v253, 0
	buffer_load_dword v226, v242, s[16:19], 0 offen sc1
	buffer_load_dword v227, v242, s[16:19], 0 offen offset:8 sc1
	buffer_load_dword v228, v242, s[16:19], 0 offen offset:16 sc1
	buffer_load_dword v229, v242, s[16:19], 0 offen offset:24 sc1
	buffer_load_dword v230, v243, s[16:19], 0 offen sc1
	buffer_load_dword v231, v243, s[16:19], 0 offen offset:8 sc1
	buffer_load_dword v232, v243, s[16:19], 0 offen offset:16 sc1
	buffer_load_dword v233, v243, s[16:19], 0 offen offset:24 sc1
	buffer_load_dword v234, v244, s[16:19], 0 offen sc1
	buffer_load_dword v235, v244, s[16:19], 0 offen offset:8 sc1
	buffer_load_dword v236, v244, s[16:19], 0 offen offset:16 sc1
	buffer_load_dword v237, v244, s[16:19], 0 offen offset:24 sc1
	buffer_load_dword v238, v245, s[16:19], 0 offen sc1
	buffer_load_dword v239, v245, s[16:19], 0 offen offset:8 sc1
	buffer_load_dword v240, v245, s[16:19], 0 offen offset:16 sc1
	buffer_load_dword v241, v245, s[16:19], 0 offen offset:24 sc1

.Lrec_w0:
	s_waitcnt vmcnt(3)
	v_bitop3_b32 v54, v226, v227, s28 bitop3:0x7e
	v_bitop3_b32 v55, v228, v229, s28 bitop3:0x7e
	v_bitop3_b32 v54, v54, v55, s34 bitop3:0xa8
	v_cmp_ne_u32_e32 vcc, 0, v54
	s_andn2_b64 vcc, vcc, s[26:27]
	s_cbranch_vccnz .Lrec_retry0
	s_cmp_eq_u32 s46, 0
	s_cbranch_scc1 .Lrec_norot
	v_accvgpr_read_b32 v43, a33
	v_accvgpr_read_b32 v42, a32
	v_accvgpr_write_b32 a33, v41
	v_accvgpr_write_b32 a32, v40
.Lrec_norot:
	s_nop 0
	v_fma_mix_f32 v246, v42, s40, v45 op_sel_hi:[1,0,0]
	v_fma_mix_f32 v247, v42, s40, v6 op_sel:[1,0,0] op_sel_hi:[1,0,0]
	v_fma_mix_f32 v248, v43, s38, v8 op_sel_hi:[1,0,0]
	v_fma_mix_f32 v249, v43, s40, v7 op_sel:[1,0,0] op_sel_hi:[1,0,0]
	v_smfmac_f32_16x16x64_f16 v[10:13], v[226:229], a[36:43], v26
	v_smfmac_f32_16x16x64_f16 v[14:17], v[226:229], a[68:75], v26
	v_smfmac_f32_16x16x64_f16 v[18:21], v[226:229], v[66:73], v26
	v_smfmac_f32_16x16x64_f16 v[22:25], v[226:229], v[98:105], v26
	v_smfmac_f32_16x16x64_f16 v[46:49], v[226:229], v[130:137], v26
	v_smfmac_f32_16x16x64_f16 v[50:53], v[226:229], v[162:169], v26
	v_smfmac_f32_16x16x64_f16 v[2:5], v[226:229], v[194:201], v26
	v_smfmac_f32_16x16x64_f16 v[250:253], v[226:229], a[120:127], v26
.Lrec_w1:
	s_waitcnt vmcnt(2)
	v_bitop3_b32 v54, v230, v231, s28 bitop3:0x7e
	v_bitop3_b32 v55, v232, v233, s28 bitop3:0x7e
	v_bitop3_b32 v54, v54, v55, s34 bitop3:0xa8
	v_cmp_ne_u32_e32 vcc, 0, v54
	s_andn2_b64 vcc, vcc, s[26:27]
	s_cbranch_vccnz .Lrec_retry1
	v_smfmac_f32_16x16x64_f16 v[10:13], v[230:233], a[44:51], v26
	v_smfmac_f32_16x16x64_f16 v[14:17], v[230:233], a[76:83], v26
	v_smfmac_f32_16x16x64_f16 v[18:21], v[230:233], v[74:81], v26
	v_smfmac_f32_16x16x64_f16 v[22:25], v[230:233], v[106:113], v26
	v_smfmac_f32_16x16x64_f16 v[46:49], v[230:233], v[138:145], v26
	v_smfmac_f32_16x16x64_f16 v[50:53], v[230:233], v[170:177], v26
	v_smfmac_f32_16x16x64_f16 v[2:5], v[230:233], v[202:209], v26
	v_smfmac_f32_16x16x64_f16 v[250:253], v[230:233], a[128:135], v26
.Lrec_w2:
	s_waitcnt vmcnt(1)
	v_bitop3_b32 v54, v234, v235, s28 bitop3:0x7e
	v_bitop3_b32 v55, v236, v237, s28 bitop3:0x7e
	v_bitop3_b32 v54, v54, v55, s34 bitop3:0xa8
	v_cmp_ne_u32_e32 vcc, 0, v54
	s_andn2_b64 vcc, vcc, s[26:27]
	s_cbranch_vccnz .Lrec_retry2
	v_smfmac_f32_16x16x64_f16 v[10:13], v[234:237], a[52:59], v26
	v_smfmac_f32_16x16x64_f16 v[14:17], v[234:237], a[84:91], v26
	v_smfmac_f32_16x16x64_f16 v[18:21], v[234:237], v[82:89], v26
	v_smfmac_f32_16x16x64_f16 v[22:25], v[234:237], v[114:121], v26
	v_smfmac_f32_16x16x64_f16 v[46:49], v[234:237], v[146:153], v26
	v_smfmac_f32_16x16x64_f16 v[50:53], v[234:237], v[178:185], v26
	v_smfmac_f32_16x16x64_f16 v[2:5], v[234:237], v[210:217], v26
	v_smfmac_f32_16x16x64_f16 v[250:253], v[234:237], a[136:143], v26
.Lrec_w3:
	s_waitcnt vmcnt(0)
	v_bitop3_b32 v54, v238, v239, s28 bitop3:0x7e
	v_bitop3_b32 v55, v240, v241, s28 bitop3:0x7e
	v_bitop3_b32 v54, v54, v55, s34 bitop3:0xa8
	v_cmp_ne_u32_e32 vcc, 0, v54
	s_andn2_b64 vcc, vcc, s[26:27]
	s_cbranch_vccnz .Lrec_retry3
	s_add_i32 s14, s46, 1
	s_lshl_b32 s6, s14, 13
	s_lshl_b32 s7, s14, 17
	s_and_b32 s6, s6, 0x8000
	s_and_b32 s7, s7, 0x60000
	v_add_u32_e32 v242, s7, v27
	v_add_u32_e32 v243, s7, v28
	v_add_u32_e32 v244, s7, v29
	v_add_u32_e32 v245, s7, v30
	v_smfmac_f32_16x16x64_f16 v[10:13], v[238:241], a[60:67], v26
	v_smfmac_f32_16x16x64_f16 v[14:17], v[238:241], v[58:65], v26
	v_smfmac_f32_16x16x64_f16 v[18:21], v[238:241], v[90:97], v26
	v_smfmac_f32_16x16x64_f16 v[22:25], v[238:241], v[122:129], v26
	v_smfmac_f32_16x16x64_f16 v[46:49], v[238:241], v[154:161], v26
	v_smfmac_f32_16x16x64_f16 v[50:53], v[238:241], v[186:193], v26
	v_smfmac_f32_16x16x64_f16 v[2:5], v[238:241], v[218:225], v26
	v_smfmac_f32_16x16x64_f16 v[250:253], v[238:241], a[112:119], v26
	s_nop 4
	v_permlane32_swap_b32_e32 v10, v46
	v_permlane32_swap_b32_e32 v14, v50
	v_permlane32_swap_b32_e32 v18, v2
	v_permlane32_swap_b32_e32 v22, v250
	v_add_f32_e32 v10, v10, v46
	v_add_f32_e32 v14, v14, v50
	v_add_f32_e32 v18, v18, v2
	v_add_f32_e32 v22, v22, v250
	ds_write_b32 v31, v10
	ds_write_b32 v31, v14 offset:64
	ds_write_b32 v35, v18
	ds_write_b32 v35, v22 offset:64
	v_permlane32_swap_b32_e32 v11, v47
	v_permlane32_swap_b32_e32 v15, v51
	v_permlane32_swap_b32_e32 v19, v3
	v_permlane32_swap_b32_e32 v23, v251
	v_add_f32_e32 v11, v11, v47
	v_add_f32_e32 v15, v15, v51
	v_add_f32_e32 v19, v19, v3
	v_add_f32_e32 v23, v23, v251
	ds_write_b32 v32, v11
	ds_write_b32 v32, v15 offset:64
	ds_write_b32 v36, v19
	ds_write_b32 v36, v23 offset:64
	v_permlane32_swap_b32_e32 v12, v48
	v_permlane32_swap_b32_e32 v16, v52
	v_permlane32_swap_b32_e32 v20, v4
	v_permlane32_swap_b32_e32 v24, v252
	v_add_f32_e32 v12, v12, v48
	v_add_f32_e32 v16, v16, v52
	v_add_f32_e32 v20, v20, v4
	v_add_f32_e32 v24, v24, v252
	ds_write_b32 v33, v12
	ds_write_b32 v33, v16 offset:64
	ds_write_b32 v37, v20
	ds_write_b32 v37, v24 offset:64
	v_permlane32_swap_b32_e32 v13, v49
	v_permlane32_swap_b32_e32 v17, v53
	v_permlane32_swap_b32_e32 v21, v5
	v_permlane32_swap_b32_e32 v25, v253
	v_add_f32_e32 v13, v13, v49
	v_add_f32_e32 v17, v17, v53
	v_add_f32_e32 v21, v21, v5
	v_add_f32_e32 v25, v25, v253
	ds_write_b32 v34, v13
	ds_write_b32 v34, v17 offset:64
	ds_write_b32 v38, v21
	ds_write_b32 v38, v25 offset:64
	s_waitcnt lgkmcnt(0)
	s_barrier
	ds_read_b128 v[10:13], v9
	ds_read_b128 v[14:17], v9 offset:4096
	ds_read_b128 v[18:21], v9 offset:8192
	ds_read_b128 v[22:25], v9 offset:12288
	s_min_u32 s29, s46, 0xfd
	s_lshl_b32 s29, s29, 19
	s_add_u32 s29, s29, s36
	v_mov_b32_e32 v54, s29
	v_add_co_u32_e32 v54, vcc, v254, v54
	s_nop 1
	v_addc_co_u32_e32 v55, vcc, 0, v255, vcc
	global_load_dwordx2 v[40:41], v[54:55], off
	s_waitcnt lgkmcnt(2)
	v_pk_add_f32 v[10:11], v[10:11], v[14:15]
	v_pk_add_f32 v[12:13], v[12:13], v[16:17]
	s_waitcnt lgkmcnt(0)
	v_pk_add_f32 v[18:19], v[18:19], v[22:23]
	v_pk_add_f32 v[20:21], v[20:21], v[24:25]
	v_pk_add_f32 v[10:11], v[10:11], v[18:19]
	v_pk_add_f32 v[12:13], v[12:13], v[20:21]
	v_fmac_f32_e32 v247, s48, v11
	v_fmac_f32_e32 v246, s48, v10
	v_fmac_f32_e32 v249, s48, v13
	v_fmac_f32_e32 v248, s47, v12
	v_exp_f32_e32 v15, v247
	v_exp_f32_e32 v14, v246
	v_exp_f32_e32 v17, v249
	v_max_f32_e32 v16, 0, v248
	v_add_f32_e32 v15, 1.0, v15
	v_add_f32_e32 v14, 1.0, v14
	v_add_f32_e32 v17, 1.0, v17
	v_rcp_f32_e32 v14, v14
	v_rcp_f32_e32 v15, v15
	v_rcp_f32_e32 v17, v17
	v_add_u32_e32 v18, s7, v1
	v_mul_f32_e32 v12, v16, v14
	v_fmac_f32_e32 v12, v44, v15
	v_max_f32_e32 v19, 0, v12
	v_mul_f32_e32 v13, v17, v19
	v_fma_mixlo_f16 v14, v13, s45, 0
	s_lshl_b32 s29, s46, 3
	v_and_b32_e32 v14, 0x7fff, v14
	s_andn2_b64 vcc, exec, s[4:5]
	v_or_b32_e32 v16, s6, v14
	s_cbranch_vccnz .Lrec_slowst
	buffer_store_short v16, v18, s[20:23], 0 offen
	s_branch .Lrec_stored

.Lrec_stored:
	s_cmpk_eq_i32 s14, 0x100
	s_cbranch_scc1 .Lrec_exit
	v_and_or_b32 v15, s29, 56, v56
	v_lshl_add_u32 v15, v15, 6, v0
	ds_write_b16 v15, v14 offset:33024
	v_mov_b32_e32 v44, v12
	v_xor_b32_e32 v31, 0x4000, v31
	v_xor_b32_e32 v32, 0x4000, v32
	v_xor_b32_e32 v33, 0x4000, v33
	v_xor_b32_e32 v34, 0x4000, v34
	v_xor_b32_e32 v35, 0x4000, v35
	v_xor_b32_e32 v36, 0x4000, v36
	v_xor_b32_e32 v37, 0x4000, v37
	v_xor_b32_e32 v38, 0x4000, v38
	v_xor_b32_e32 v9, 0x4000, v9
	v_mov_b32_e32 v10, 0
	v_mov_b32_e32 v11, 0
	v_mov_b32_e32 v12, 0
	v_mov_b32_e32 v13, 0
	v_mov_b32_e32 v14, 0
	v_mov_b32_e32 v15, 0
	v_mov_b32_e32 v16, 0
	v_mov_b32_e32 v17, 0
	v_mov_b32_e32 v18, 0
	v_mov_b32_e32 v19, 0
	v_mov_b32_e32 v20, 0
	v_mov_b32_e32 v21, 0
	v_mov_b32_e32 v22, 0
	v_mov_b32_e32 v23, 0
	v_mov_b32_e32 v24, 0
	v_mov_b32_e32 v25, 0
	v_mov_b32_e32 v2, 0
	v_mov_b32_e32 v3, 0
	v_mov_b32_e32 v4, 0
	v_mov_b32_e32 v5, 0
	v_mov_b32_e32 v250, 0
	v_mov_b32_e32 v251, 0
	v_mov_b32_e32 v252, 0
	v_mov_b32_e32 v253, 0
	s_sleep 3
	buffer_load_dwordx4 v[226:229], v242, s[20:23], 0 offen sc1
	buffer_load_dwordx4 v[230:233], v243, s[20:23], 0 offen sc1
	buffer_load_dwordx4 v[234:237], v244, s[20:23], 0 offen sc1
	buffer_load_dwordx4 v[238:241], v245, s[20:23], 0 offen sc1
	s_mov_b64 s[26:27], s[24:25]
	s_cmp_eq_u64 s[2:3], 0
	s_cbranch_scc1 .Lrec_noflush
	s_and_b32 s29, s46, 3
	s_cmp_lg_u32 s29, 0
	s_cbranch_scc1 .Lrec_noflush
	s_cmp_lt_u32 s46, 4
	s_cbranch_scc1 .Lrec_noflush
	s_add_i32 s29, s46, -4
	v_accvgpr_read_b32 v46, a94
	v_or_b32_e32 v50, s29, v46
	v_lshlrev_b32_e32 v46, 3, v50
	v_accvgpr_read_b32 v47, a95
	v_and_or_b32 v46, v46, 40, v47
	v_accvgpr_read_b32 v47, a96
	v_lshl_add_u32 v47, v47, 1, 0
	v_lshl_add_u32 v54, v46, 6, v47
	ds_read_b128 v[46:49], v54 offset:33024
	v_ashrrev_i32_e32 v51, 31, v50
	v_accvgpr_read_b32 v52, a100
	v_lshlrev_b64 v[50:51], 17, v[50:51]
	v_accvgpr_read_b32 v53, a101
	v_lshl_add_u64 v[50:51], v[52:53], 0, v[50:51]
	v_add_co_u32_e32 v52, vcc, 0x20000, v50
	s_nop 1
	v_addc_co_u32_e32 v53, vcc, 0, v51, vcc
	s_waitcnt lgkmcnt(0)
	global_store_dwordx4 v[52:53], v[46:49], off
	s_nop 1
	ds_read_b128 v[46:49], v54 offset:34048
	v_add_co_u32_e32 v50, vcc, 0x60000, v50
	s_nop 1
	v_addc_co_u32_e32 v51, vcc, 0, v51, vcc
	s_waitcnt lgkmcnt(0)
	global_store_dwordx4 v[50:51], v[46:49], off
	s_nop 1
.Lrec_noflush:
	v_mov_b32_e32 v10, 0
	v_mov_b32_e32 v11, 0
	v_mov_b32_e32 v12, 0
	v_mov_b32_e32 v13, 0
	v_mov_b32_e32 v14, 0
	v_mov_b32_e32 v15, 0
	v_mov_b32_e32 v16, 0
	v_mov_b32_e32 v17, 0
	v_mov_b32_e32 v18, 0
	v_mov_b32_e32 v19, 0
	v_mov_b32_e32 v20, 0
	v_mov_b32_e32 v21, 0
	v_mov_b32_e32 v22, 0
	v_mov_b32_e32 v23, 0
	v_mov_b32_e32 v24, 0
	v_mov_b32_e32 v25, 0
	v_mov_b32_e32 v46, 0
	v_mov_b32_e32 v47, 0
	v_mov_b32_e32 v48, 0
	v_mov_b32_e32 v49, 0
	v_mov_b32_e32 v50, 0
	v_mov_b32_e32 v51, 0
	v_mov_b32_e32 v52, 0
	v_mov_b32_e32 v53, 0
	v_mov_b32_e32 v2, 0
	v_mov_b32_e32 v3, 0
	v_mov_b32_e32 v4, 0
	v_mov_b32_e32 v5, 0
	v_mov_b32_e32 v250, 0
	v_mov_b32_e32 v251, 0
	v_mov_b32_e32 v252, 0
	v_mov_b32_e32 v253, 0
	s_mov_b32 s46, s14
	s_branch .Lrec_step
